# MP0 index prefetch: two global_load_dwordx3 (one per graph row) replace six strided dword loads; 7 address VALU ops dropped, 6 moves after the counted wait; vmcnt(14)->(10)
# baseline (speedup 1.0000x reference)
.LBB5_11:
	v_lshl_or_b32 v219, v219, 8, v191
	s_add_i32 m0, s24, s33
	ds_read_b128 v[226:229], v223 offset:0x3000
	s_waitcnt lgkmcnt(6)
	s_waitcnt lgkmcnt(3)
	ds_read_b128 v[230:233], v143 offset:0x3000
	s_waitcnt lgkmcnt(6)
	s_nop 0
	global_load_lds_dwordx4 v219, s[12:13]
	v_exp_f32_e32 v143, v156
	v_exp_f32_e32 v152, v152
	v_mfma_f32_16x16x32_f16 v[180:183], v[6:9], v[160:163], v[180:183]
	v_lshl_or_b32 v156, v207, 8, v191
	v_add_f32_e32 v143, 1.0, v143
	v_rcp_f32_e32 v143, v143
	v_mfma_f32_16x16x32_f16 v[176:179], v[46:49], v[160:163], v[176:179]
	v_add_u32_e32 v207, 0x3000, v225
	v_fma_f32 v143, v143, v148, v144
	v_exp_f32_e32 v148, v157
	v_exp_f32_e32 v143, v143
	v_mfma_f32_16x16x32_f16 v[160:163], v[70:73], v[160:163], v[184:187]
	v_add_f32_e32 v144, 1.0, v152
	v_add_f32_e32 v148, 1.0, v148
	v_rcp_f32_e32 v148, v148
	v_add_f32_e32 v143, 1.0, v143
	v_rcp_f32_e32 v143, v143
	v_mfma_f32_16x16x32_f16 v[180:183], v[50:53], v[164:167], v[180:183]
	v_fma_f32 v145, v148, v149, v145
	v_rcp_f32_e32 v144, v144
	v_exp_f32_e32 v152, v153
	v_mfma_f32_16x16x32_f16 v[176:179], v[18:21], v[164:167], v[176:179]
	v_fma_f32 v143, v143, -2.0, 1.0
	v_fma_f32 v143, -v144, v143, v143
	v_fma_mixlo_f16 v184, v144, v188, v143 op_sel_hi:[0,1,0]
	v_mfma_f32_16x16x32_f16 v[160:163], v[74:77], v[164:167], v[160:163]
	ds_read_b128 v[164:167], v142 offset:0x3000
	v_exp_f32_e32 v142, v145
	v_add_f32_e32 v143, 1.0, v152
	s_waitcnt lgkmcnt(6)
	v_rcp_f32_e32 v186, v143
	v_add_f32_e32 v142, 1.0, v142
	v_rcp_f32_e32 v148, v142
	v_mfma_f32_16x16x32_f16 v[142:145], v[90:93], v[168:171], v[160:163]
	v_fma_f32 v148, v148, -2.0, 1.0
	v_mfma_f32_16x16x32_f16 v[180:183], v[10:13], v[168:171], v[180:183]
	v_fma_f32 v187, -v186, v148, v148
	v_mfma_f32_16x16x32_f16 v[176:179], v[58:61], v[168:171], v[176:179]
	s_add_i32 m0, s34, 0x4000
	s_waitcnt lgkmcnt(3)
	s_waitcnt lgkmcnt(2)
	v_exp_f32_e32 v148, v158
	global_load_lds_dwordx4 v156, s[12:13]
	v_exp_f32_e32 v149, v154
	v_add_f32_e32 v148, 1.0, v148
	v_rcp_f32_e32 v148, v148
	v_mfma_f32_16x16x32_f16 v[160:163], v[14:17], v[172:175], v[180:183]
	s_waitcnt lgkmcnt(1)
	s_waitcnt lgkmcnt(0)
	v_fma_f32 v146, v148, v150, v146
	v_add_f32_e32 v148, 1.0, v149
	v_exp_f32_e32 v146, v146
	v_rcp_f32_e32 v150, v148
	v_exp_f32_e32 v148, v159
	v_mfma_f32_16x16x32_f16 v[168:171], v[22:25], v[172:175], v[176:179]
	v_add_f32_e32 v146, 1.0, v146
	v_rcp_f32_e32 v146, v146
	v_add_f32_e32 v148, 1.0, v148
	v_rcp_f32_e32 v148, v148
	v_mfma_f32_16x16x32_f16 v[172:175], v[86:89], v[172:175], v[130:133]
	v_fma_f32 v146, v146, -2.0, 1.0
	v_fma_mixhi_f16 v184, v186, v188, v187 op_sel:[0,1,0] op_sel_hi:[0,1,0]
	v_fmac_f32_e32 v147, v148, v151
	v_mfma_f32_16x16x32_f16 v[160:163], v[26:29], v[226:229], v[160:163]
	v_exp_f32_e32 v147, v147
	v_mfma_f32_16x16x32_f16 v[156:159], v[78:81], v[226:229], v[172:175]
	s_nop 2
	v_fma_f32 v172, -v150, v146, v146
	v_exp_f32_e32 v146, v155
	v_mfma_f32_16x16x32_f16 v[168:171], v[34:37], v[226:229], v[168:171]
	v_fma_mixlo_f16 v185, v150, v189, v172 op_sel_hi:[0,1,0]
	v_add_f32_e32 v151, 1.0, v146
	v_mfma_f32_16x16x32_f16 v[160:163], v[30:33], v[230:233], v[160:163]
	v_add_f32_e32 v146, 1.0, v147
	v_mfma_f32_16x16x32_f16 v[152:155], v[38:41], v[230:233], v[168:171]
	s_nop 2
	v_rcp_f32_e32 v168, v146
	v_mfma_f32_16x16x32_f16 v[146:149], v[54:57], v[164:167], v[160:163]
	s_nop 2
	v_rcp_f32_e32 v160, v151
	v_mfma_f32_16x16x32_f16 v[156:159], v[82:85], v[230:233], v[156:159]
	v_fma_f32 v161, v168, -2.0, 1.0
	v_mfma_f32_16x16x32_f16 v[150:153], v[62:65], v[164:167], v[152:155]
	s_nop 2
	v_fma_f32 v154, -v160, v161, v161
	v_fma_mixhi_f16 v185, v160, v189, v154 op_sel:[0,1,0] op_sel_hi:[0,1,0]
	v_mfma_f32_16x16x32_f16 v[154:157], v[94:97], v[164:167], v[156:159]
	global_store_dwordx2 v207, v[184:185], s[0:1] nt
	s_add_i32 s27, s27, 1
	s_add_i32 s20, s20, s30
	s_waitcnt lgkmcnt(0)
	s_waitcnt vmcnt(11)
	v_mov_b32_e32 v193, v244
	v_mov_b32_e32 v192, v245
	v_mov_b32_e32 v196, v246
	v_mov_b32_e32 v222, v248
	v_mov_b32_e32 v221, v249
	v_mov_b32_e32 v194, v250
	v_add_u32_e32 v213, s29, v213
	v_add_u32_e32 v215, s31, v215
	v_add_u32_e32 v217, s29, v217
	s_cmp_lt_i32 s2, s9
	v_mov_b32_e32 v207, v221
	v_mov_b32_e32 v219, v222
	s_cbranch_scc0 .LBB5_16

.LBB5_14:
	v_or_b32_e32 v0, s33, v200
	ds_read_b128 v[142:145], v0 offset:0
	s_waitcnt lgkmcnt(4)
	s_nop 0
	v_mfma_f32_16x16x32_f16 v[134:137], v[114:117], v[134:137], v[166:169]
	ds_read_b128 v[146:149], v0 offset:0x1000
	s_waitcnt lgkmcnt(4)
	s_nop 0
	v_mfma_f32_16x16x32_f16 v[138:141], v[114:117], v[138:141], v[170:173]
	ds_read_b128 v[150:153], v0 offset:0x2000
	s_waitcnt lgkmcnt(4)
	s_nop 0
	v_mfma_f32_16x16x32_f16 v[154:157], v[114:117], v[158:161], v[174:177]
	ds_read_b128 v[158:161], v0 offset:0x3000
	s_waitcnt lgkmcnt(4)
	s_nop 0
	v_mfma_f32_16x16x32_f16 v[162:165], v[114:117], v[162:165], v[178:181]
	ds_read_b128 v[166:169], v205 offset:0
	s_waitcnt lgkmcnt(4)
	s_nop 0
	v_mfma_f32_16x16x32_f16 v[134:137], v[106:109], v[142:145], v[134:137]
	ds_read_b128 v[142:145], v205 offset:0x100
	s_waitcnt lgkmcnt(4)
	s_nop 0
	v_mfma_f32_16x16x32_f16 v[138:141], v[106:109], v[146:149], v[138:141]
	ds_read_b128 v[146:149], v205 offset:0x200
	s_waitcnt lgkmcnt(4)
	s_nop 0
	v_mfma_f32_16x16x32_f16 v[150:153], v[106:109], v[150:153], v[154:157]
	ds_read_b128 v[154:157], v205 offset:0x300
	s_waitcnt lgkmcnt(4)
	s_nop 0
	v_mfma_f32_16x16x32_f16 v[158:161], v[106:109], v[158:161], v[162:165]
	s_waitcnt lgkmcnt(3)
	s_nop 0
	v_mfma_f32_16x16x32_f16 v[134:137], v[102:105], v[166:169], v[134:137]
	s_waitcnt lgkmcnt(2)
	s_nop 0
	v_mfma_f32_16x16x32_f16 v[138:141], v[102:105], v[142:145], v[138:141]
	s_waitcnt lgkmcnt(1)
	s_nop 0
	v_mfma_f32_16x16x32_f16 v[142:145], v[102:105], v[146:149], v[150:153]
	s_waitcnt lgkmcnt(0)
	s_nop 0
	v_mfma_f32_16x16x32_f16 v[146:149], v[102:105], v[154:157], v[158:161]
	s_nop 1
	v_cvt_pk_f16_f32 v1, v136, v137
	v_pk_max_f16 v1, v1, 0
	v_cvt_pk_f16_f32 v0, v134, v135
	v_pk_max_f16 v0, v0, 0
	v_cvt_pk_f16_f32 v135, v140, v141
	v_pk_max_f16 v135, v135, 0
	v_cvt_pk_f16_f32 v134, v138, v139
	v_pk_max_f16 v134, v134, 0
	ds_write2st64_b64 v218, v[0:1], v[134:135] offset1:8
	v_cvt_pk_f16_f32 v1, v144, v145
	v_pk_max_f16 v1, v1, 0
	v_cvt_pk_f16_f32 v0, v142, v143
	v_pk_max_f16 v0, v0, 0
	s_lshl_b32 s34, s2, 14
	v_cvt_pk_f16_f32 v135, v148, v149
	v_pk_max_f16 v135, v135, 0
	v_cvt_pk_f16_f32 v134, v146, v147
	v_pk_max_f16 v134, v134, 0
	s_or_b32 s34, s34, 0x18000
	ds_write2st64_b64 v218, v[0:1], v[134:135] offset0:16 offset1:24
	v_or_b32_e32 v172, s34, v197
	v_or_b32_e32 v223, s34, v198
	v_or_b32_e32 v143, s34, v199
	v_or_b32_e32 v142, s34, v200
	v_add_u32_e32 v0, s34, v208
	s_xor_b32 s34, s2, 1
	s_waitcnt vmcnt(2) lgkmcnt(0)
	s_barrier
	ds_read_b128 v[134:137], v201 offset:0
	s_mul_i32 s37, s34, 0xc000
	ds_read_b128 v[138:141], v202 offset:0
	ds_read_b128 v[144:147], v203 offset:0
	ds_read_b128 v[148:151], v204 offset:0
	v_add_u32_e32 v1, s37, v209
	ds_read_b128 v[152:155], v1 offset:0
	ds_read_b128 v[156:159], v1 offset:0x4000
	ds_read_b128 v[160:163], v1 offset:0x8000
	ds_read_b128 v[164:167], v1 offset:0x400
	ds_read_b128 v[168:171], v1 offset:0x4400
	ds_read_b128 v[174:177], v1 offset:0x8400
	ds_read_b128 v[178:181], v172 offset:0
	s_waitcnt lgkmcnt(10)
	v_subrev_u32_e32 v186, 56, v215
	v_mfma_f32_16x16x32_f16 v[182:185], v[2:5], v[134:137], v[118:121]
	v_min_u32_e32 v225, s17, v186
	v_mfma_f32_16x16x32_f16 v[186:189], v[42:45], v[134:137], v[122:125]
	ds_read_b128 v[226:229], v223 offset:0
	s_waitcnt lgkmcnt(10)
	v_mfma_f32_16x16x32_f16 v[134:137], v[66:69], v[134:137], v[126:129]
	v_lshl_or_b32 v173, v196, 8, v190
	v_mfma_f32_16x16x32_f16 v[182:185], v[6:9], v[138:141], v[182:185]
	v_add_u32_e32 v196, -8, v215
	v_min_u32_e32 v238, s17, v196
	v_mfma_f32_16x16x32_f16 v[186:189], v[46:49], v[138:141], v[186:189]
	v_mfma_f32_16x16x32_f16 v[230:233], v[70:73], v[138:141], v[134:137]
	s_cmp_lg_u32 s42, 0
	s_cbranch_scc1 .Lmp0_nofeat
	v_add_u32_e32 v224, s20, v216
	v_cmp_gt_u32_e32 vcc, s8, v224
	v_mov_b32_e32 v234, s16
	s_nop 0
	v_cndmask_b32_e32 v234, v234, v224, vcc
	v_lshlrev_b32_e32 v234, 5, v234
	global_load_dwordx4 v[134:137], v234, s[6:7]
	global_load_dwordx4 v[138:141], v234, s[6:7] offset:16
.Lmp0_nofeat:
	ds_read_b128 v[234:237], v143 offset:0
	s_waitcnt lgkmcnt(10)
	v_lshl_or_b32 v242, v192, 8, v190
	v_mfma_f32_16x16x32_f16 v[182:185], v[50:53], v[144:147], v[182:185]
	v_mfma_f32_16x16x32_f16 v[186:189], v[18:21], v[144:147], v[186:189]
	v_lshl_or_b32 v241, v194, 8, v191
	v_mfma_f32_16x16x32_f16 v[144:147], v[74:77], v[144:147], v[230:233]
	ds_read_b128 v[230:233], v142 offset:0
	s_waitcnt lgkmcnt(10)
	s_add_i32 s2, s28, s3
	v_mfma_f32_16x16x32_f16 v[182:185], v[10:13], v[148:151], v[182:185]
	v_lshl_or_b32 v243, v193, 8, v190
	global_load_dwordx3 v[244:246], v225, s[4:5]
	s_min_i32 s35, s2, s14
	v_mfma_f32_16x16x32_f16 v[186:189], v[58:61], v[148:151], v[186:189]
	global_load_dwordx3 v[248:250], v238, s[4:5]
	s_lshl_b32 s35, s35, 14
	s_lshl_b32 s34, s34, 14
	v_mfma_f32_16x16x32_f16 v[148:151], v[90:93], v[148:151], v[144:147]
	s_add_i32 s36, s33, 0
	v_add_u32_e32 v1, s35, v210
	s_add_i32 s38, s25, s34
	s_add_i32 s39, s36, s21
	s_add_i32 s40, s26, s34
	s_add_i32 s34, s36, s23
	s_add_i32 m0, s39, 0x8000
	v_add_u32_e32 v240, s35, v211
	s_add_i32 s41, s34, 0x8000
	s_add_i32 s35, s39, 0x4000
	s_add_i32 s36, s22, s33
	v_add_u32_e32 v239, s37, v212
	ds_read_b128 v[144:147], v201 offset:0x1000
	s_waitcnt lgkmcnt(4)
	s_waitcnt lgkmcnt(5)
	s_nop 0
	v_pk_add_f16 v152, v152, v156
	v_pk_add_f16 v153, v153, v157
	v_pk_add_f16 v154, v154, v158
	v_pk_add_f16 v155, v155, v159
	v_pk_add_f16 v154, v154, v162
	v_pk_add_f16 v155, v155, v163
	v_pk_add_f16 v153, v153, v161
	v_pk_add_f16 v152, v152, v160
	ds_write_b128 v239, v[152:155]
	v_pk_add_f16 v152, v164, v168
	v_pk_add_f16 v153, v165, v169
	v_pk_add_f16 v154, v166, v170
	v_pk_add_f16 v155, v167, v171
	v_pk_add_f16 v154, v154, v176
	v_pk_add_f16 v155, v155, v177
	v_pk_add_f16 v153, v153, v175
	v_pk_add_f16 v152, v152, v174
	ds_write_b128 v239, v[152:155] offset:1024
	ds_read_b128 v[152:155], v202 offset:0x1000
	s_waitcnt lgkmcnt(4)
	global_load_lds_dwordx4 v173, s[12:13]
	s_mov_b32 m0, s38
	ds_read_b128 v[168:171], v203 offset:0x1000
	s_waitcnt lgkmcnt(4)
	v_mfma_f32_16x16x32_f16 v[182:185], v[14:17], v[178:181], v[182:185]
	global_load_lds_dwordx4 v1, s[12:13]
	ds_read_b128 v[174:177], v204 offset:0x1000
	v_mfma_f32_16x16x32_f16 v[186:189], v[22:25], v[178:181], v[186:189]
	s_waitcnt lgkmcnt(4)
	v_mfma_f32_16x16x32_f16 v[178:181], v[86:89], v[178:181], v[130:133]
	v_mfma_f32_16x16x32_f16 v[156:159], v[26:29], v[226:229], v[182:185]
	v_mfma_f32_16x16x32_f16 v[160:163], v[34:37], v[226:229], v[186:189]
	v_mfma_f32_16x16x32_f16 v[164:167], v[78:81], v[226:229], v[178:181]
	v_mfma_f32_16x16x32_f16 v[156:159], v[30:33], v[234:237], v[156:159]
	v_mfma_f32_16x16x32_f16 v[160:163], v[38:41], v[234:237], v[160:163]
	v_mfma_f32_16x16x32_f16 v[164:167], v[82:85], v[234:237], v[164:167]
	v_mfma_f32_16x16x32_f16 v[156:159], v[54:57], v[230:233], v[156:159]
	v_mfma_f32_16x16x32_f16 v[160:163], v[62:65], v[230:233], v[160:163]
	v_mfma_f32_16x16x32_f16 v[164:167], v[94:97], v[230:233], v[164:167]
	s_mov_b32 m0, s41
	ds_read_b64 v[234:235], v0 offset:0
	ds_read_b128 v[178:181], v172 offset:0x1000
	s_waitcnt lgkmcnt(5)
	ds_read_b128 v[186:189], v223 offset:0x1000
	s_waitcnt lgkmcnt(5)
	s_nop 4
	v_exp_f32_e32 v1, v156
	s_waitcnt lgkmcnt(2)
	ds_read_b128 v[230:233], v143 offset:0x1000
	s_waitcnt lgkmcnt(5)
	global_load_lds_dwordx4 v241, s[12:13]
	v_add_f32_e32 v1, 1.0, v1
	v_rcp_f32_e32 v1, v1
	v_exp_f32_e32 v156, v160
	v_mfma_f32_16x16x32_f16 v[182:185], v[2:5], v[144:147], v[118:121]
	v_add_u32_e32 v225, v206, v213
	v_fma_f32 v1, v1, v164, v148
	v_exp_f32_e32 v1, v1
	v_add_f32_e32 v148, 1.0, v156
	v_exp_f32_e32 v156, v157
	v_rcp_f32_e32 v148, v148
	v_add_f32_e32 v1, 1.0, v1
	v_rcp_f32_e32 v1, v1
	v_add_f32_e32 v156, 1.0, v156
	v_rcp_f32_e32 v156, v156
	v_mfma_f32_16x16x32_f16 v[226:229], v[42:45], v[144:147], v[122:125]
	v_fma_f32 v1, v1, -2.0, 1.0
	v_fma_f32 v1, -v148, v1, v1
	v_fma_mixlo_f16 v1, v148, v234, v1 op_sel_hi:[0,1,0]
	v_mfma_f32_16x16x32_f16 v[144:147], v[66:69], v[144:147], v[126:129]
	v_exp_f32_e32 v148, v161
	v_fma_f32 v149, v156, v165, v149
	v_exp_f32_e32 v149, v149
	v_mfma_f32_16x16x32_f16 v[182:185], v[6:9], v[152:155], v[182:185]
	v_add_f32_e32 v148, 1.0, v148
	v_rcp_f32_e32 v156, v148
	v_add_f32_e32 v148, 1.0, v149
	v_mfma_f32_16x16x32_f16 v[226:229], v[46:49], v[152:155], v[226:229]
	v_rcp_f32_e32 v157, v148
	v_add_u32_e32 v173, 0x1000, v225
	v_mfma_f32_16x16x32_f16 v[144:147], v[70:73], v[152:155], v[144:147]
	v_mfma_f32_16x16x32_f16 v[152:155], v[50:53], v[168:171], v[182:185]
	v_mfma_f32_16x16x32_f16 v[182:185], v[18:21], v[168:171], v[226:229]
	v_mfma_f32_16x16x32_f16 v[144:147], v[74:77], v[168:171], v[144:147]
	ds_read_b128 v[168:171], v142 offset:0x1000
	s_waitcnt lgkmcnt(5)
	s_nop 0
	v_mfma_f32_16x16x32_f16 v[152:155], v[10:13], v[174:177], v[152:155]
	v_mfma_f32_16x16x32_f16 v[182:185], v[58:61], v[174:177], v[182:185]
	v_mfma_f32_16x16x32_f16 v[146:149], v[90:93], v[174:177], v[144:147]
	s_nop 3
	v_fma_f32 v144, v157, -2.0, 1.0
	v_fma_f32 v144, -v156, v144, v144
	v_fma_mixlo_f16 v144, v156, v234, v144 op_sel:[0,1,0] op_sel_hi:[0,1,0]
	s_mov_b32 m0, s40
	ds_read_b128 v[174:177], v201 offset:0x2000
	s_waitcnt lgkmcnt(4)
	ds_read_b128 v[226:229], v202 offset:0x2000
	s_waitcnt lgkmcnt(4)
	v_exp_f32_e32 v145, v158
	global_load_lds_dwordx4 v240, s[12:13]
	v_exp_f32_e32 v156, v162
	v_add_f32_e32 v145, 1.0, v145
	v_rcp_f32_e32 v145, v145
	v_mfma_f32_16x16x32_f16 v[152:155], v[14:17], v[178:181], v[152:155]
	v_pack_b32_f16 v144, v1, v144
	v_fma_f32 v145, v145, v166, v150
	v_add_f32_e32 v150, 1.0, v156
	v_rcp_f32_e32 v234, v150
	v_exp_f32_e32 v150, v159
	v_mfma_f32_16x16x32_f16 v[182:185], v[22:25], v[178:181], v[182:185]
	v_exp_f32_e32 v145, v145
	v_add_f32_e32 v150, 1.0, v150
	v_mfma_f32_16x16x32_f16 v[178:181], v[86:89], v[178:181], v[130:133]
	v_rcp_f32_e32 v150, v150
	v_add_f32_e32 v145, 1.0, v145
	v_rcp_f32_e32 v145, v145
	v_mfma_f32_16x16x32_f16 v[182:185], v[34:37], v[186:189], v[182:185]
	v_fmac_f32_e32 v151, v150, v167
	v_fma_f32 v145, v145, -2.0, 1.0
	v_mfma_f32_16x16x32_f16 v[178:181], v[78:81], v[186:189], v[178:181]
	v_fma_f32 v145, -v234, v145, v145
	v_fma_mixlo_f16 v145, v234, v235, v145 op_sel_hi:[0,1,0]
	v_mfma_f32_16x16x32_f16 v[152:155], v[26:29], v[186:189], v[152:155]
	ds_read_b128 v[186:189], v203 offset:0x2000
	s_waitcnt lgkmcnt(4)
	ds_read_b128 v[164:167], v204 offset:0x2000
	s_waitcnt lgkmcnt(4)
	s_nop 0
	v_mfma_f32_16x16x32_f16 v[156:159], v[38:41], v[230:233], v[182:185]
	s_nop 2
	v_exp_f32_e32 v182, v163
	v_mfma_f32_16x16x32_f16 v[160:163], v[82:85], v[230:233], v[178:181]
	s_nop 2
	v_exp_f32_e32 v178, v151
	v_mfma_f32_16x16x32_f16 v[152:155], v[30:33], v[230:233], v[152:155]
	v_add_f32_e32 v179, 1.0, v182
	v_add_f32_e32 v178, 1.0, v178
	v_mfma_f32_16x16x32_f16 v[150:153], v[54:57], v[168:171], v[152:155]
	v_mfma_f32_16x16x32_f16 v[154:157], v[62:65], v[168:171], v[156:159]
	s_nop 2
	v_rcp_f32_e32 v158, v178
	v_rcp_f32_e32 v159, v179
	v_mfma_f32_16x16x32_f16 v[168:171], v[94:97], v[168:171], v[160:163]
	v_fma_f32 v158, v158, -2.0, 1.0
	v_fma_f32 v158, -v159, v158, v158
	v_fma_mixlo_f16 v158, v159, v235, v158 op_sel:[0,1,0] op_sel_hi:[0,1,0]
	s_nop 0
	v_pack_b32_f16 v145, v145, v158
	global_store_dwordx2 v173, v[144:145], s[0:1] nt
	s_mov_b32 m0, s36
	ds_read_b64 v[238:239], v0 offset:0x1000
	ds_read_b128 v[178:181], v172 offset:0x2000
	s_waitcnt lgkmcnt(5)
	ds_read_b128 v[182:185], v223 offset:0x2000
	s_waitcnt lgkmcnt(5)
	v_exp_f32_e32 v1, v150
	s_waitcnt lgkmcnt(2)
	ds_read_b128 v[234:237], v143 offset:0x2000
	s_waitcnt lgkmcnt(5)
	global_load_lds_dwordx4 v243, s[12:13]
	v_add_f32_e32 v1, 1.0, v1
	v_rcp_f32_e32 v1, v1
	v_exp_f32_e32 v145, v151
	v_mfma_f32_16x16x32_f16 v[158:161], v[2:5], v[174:177], v[118:121]
	v_exp_f32_e32 v144, v154
	v_fma_f32 v1, v1, v168, v146
	v_exp_f32_e32 v1, v1
	v_mfma_f32_16x16x32_f16 v[230:233], v[42:45], v[174:177], v[122:125]
	v_add_f32_e32 v145, 1.0, v145
	v_rcp_f32_e32 v145, v145
	v_add_f32_e32 v1, 1.0, v1
	v_mfma_f32_16x16x32_f16 v[174:177], v[66:69], v[174:177], v[126:129]
	v_add_f32_e32 v144, 1.0, v144
	v_rcp_f32_e32 v1, v1
	v_rcp_f32_e32 v144, v144
	v_mfma_f32_16x16x32_f16 v[158:161], v[6:9], v[226:229], v[158:161]
	v_fma_f32 v145, v145, v169, v147
	v_exp_f32_e32 v145, v145
	v_exp_f32_e32 v146, v155
	v_mfma_f32_16x16x32_f16 v[174:177], v[70:73], v[226:229], v[174:177]
	v_fma_f32 v1, v1, -2.0, 1.0
	v_fma_f32 v1, -v144, v1, v1
	v_fma_mixlo_f16 v240, v144, v238, v1 op_sel_hi:[0,1,0]
	v_mfma_f32_16x16x32_f16 v[230:233], v[46:49], v[226:229], v[230:233]
	v_add_f32_e32 v144, 1.0, v145
	v_add_f32_e32 v1, 1.0, v146
	v_rcp_f32_e32 v150, v144
	v_mfma_f32_16x16x32_f16 v[158:161], v[50:53], v[186:189], v[158:161]
	v_rcp_f32_e32 v1, v1
	v_add_u32_e32 v173, 0x2000, v225
	v_fma_f32 v150, v150, -2.0, 1.0
	v_mfma_f32_16x16x32_f16 v[174:177], v[74:77], v[186:189], v[174:177]
	v_fma_f32 v243, -v1, v150, v150
	v_mfma_f32_16x16x32_f16 v[226:229], v[18:21], v[186:189], v[230:233]
	ds_read_b128 v[186:189], v142 offset:0x2000
	s_waitcnt lgkmcnt(5)
	s_nop 0
	v_mfma_f32_16x16x32_f16 v[158:161], v[10:13], v[164:167], v[158:161]
	v_mfma_f32_16x16x32_f16 v[144:147], v[90:93], v[164:167], v[174:177]
	v_mfma_f32_16x16x32_f16 v[226:229], v[58:61], v[164:167], v[226:229]
	s_mov_b32 m0, s35
	ds_read_b128 v[230:233], v201 offset:0x3000
	s_waitcnt lgkmcnt(4)
	v_exp_f32_e32 v150, v152
	v_mfma_f32_16x16x32_f16 v[164:167], v[14:17], v[178:181], v[158:161]
	ds_read_b128 v[160:163], v202 offset:0x3000
	s_waitcnt lgkmcnt(4)
	global_load_lds_dwordx4 v242, s[12:13]
	v_exp_f32_e32 v154, v153
	v_add_f32_e32 v150, 1.0, v150
	v_rcp_f32_e32 v150, v150
	v_mfma_f32_16x16x32_f16 v[174:177], v[22:25], v[178:181], v[226:229]
	v_add_f32_e32 v154, 1.0, v154
	v_rcp_f32_e32 v154, v154
	v_exp_f32_e32 v151, v156
	v_mfma_f32_16x16x32_f16 v[178:181], v[86:89], v[178:181], v[130:133]
	v_fma_f32 v148, v150, v170, v148
	v_exp_f32_e32 v148, v148
	v_fmac_f32_e32 v149, v154, v171
	v_mfma_f32_16x16x32_f16 v[226:229], v[26:29], v[182:185], v[164:167]
	v_exp_f32_e32 v149, v149
	v_add_f32_e32 v150, 1.0, v151
	v_rcp_f32_e32 v241, v150
	v_mfma_f32_16x16x32_f16 v[174:177], v[34:37], v[182:185], v[174:177]
	v_add_f32_e32 v148, 1.0, v148
	ds_read_b128 v[164:167], v203 offset:0x3000
	s_waitcnt lgkmcnt(4)
	v_mfma_f32_16x16x32_f16 v[178:181], v[78:81], v[182:185], v[178:181]
	v_exp_f32_e32 v155, v157
	v_rcp_f32_e32 v148, v148
	v_add_f32_e32 v149, 1.0, v149
	v_mfma_f32_16x16x32_f16 v[150:153], v[30:33], v[234:237], v[226:229]
	v_rcp_f32_e32 v149, v149
	ds_read_b128 v[168:171], v204 offset:0x3000
	s_waitcnt lgkmcnt(4)
	v_mfma_f32_16x16x32_f16 v[174:177], v[38:41], v[234:237], v[174:177]
	v_fma_f32 v148, v148, -2.0, 1.0
	v_fma_f32 v148, -v241, v148, v148
	v_fma_mixlo_f16 v241, v241, v239, v148 op_sel_hi:[0,1,0]
	v_mfma_f32_16x16x32_f16 v[178:181], v[82:85], v[234:237], v[178:181]
	v_fma_mixhi_f16 v240, v1, v238, v243 op_sel:[0,1,0] op_sel_hi:[0,1,0]
	v_mfma_f32_16x16x32_f16 v[156:159], v[54:57], v[186:189], v[150:153]
	s_nop 2
	v_add_f32_e32 v150, 1.0, v155
	v_mfma_f32_16x16x32_f16 v[152:155], v[62:65], v[186:189], v[174:177]
	s_nop 2
	v_rcp_f32_e32 v174, v150
	v_fma_f32 v175, v149, -2.0, 1.0
	v_mfma_f32_16x16x32_f16 v[148:151], v[94:97], v[186:189], v[178:181]
	v_fma_f32 v175, -v174, v175, v175
	v_fma_mixhi_f16 v241, v174, v239, v175 op_sel:[0,1,0] op_sel_hi:[0,1,0]
	global_store_dwordx2 v173, v[240:241], s[0:1] nt
	ds_read_b64 v[188:189], v0 offset:0x2000
	ds_read_b64 v[0:1], v0 offset:0x3000
	ds_read_b128 v[172:175], v172 offset:0x3000
	s_waitcnt lgkmcnt(6)
	s_andn2_b64 vcc, exec, s[10:11]
	v_mfma_f32_16x16x32_f16 v[180:183], v[2:5], v[230:233], v[118:121]
	s_waitcnt vmcnt(10)
	v_mfma_f32_16x16x32_f16 v[176:179], v[42:45], v[230:233], v[122:125]
	v_mfma_f32_16x16x32_f16 v[184:187], v[66:69], v[230:233], v[126:129]
	s_cbranch_vccnz .LBB5_11
	v_cvt_pk_f16_f32 v226, v134, v135
	v_cvt_pk_f16_f32 v227, v136, v137
	v_cvt_pk_f16_f32 v228, v138, v139
	v_cvt_pk_f16_f32 v229, v140, v141
	s_add_i32 s46, s20, s30
	s_add_i32 s46, s46, 63
	s_cmp_lt_i32 s46, s8
	s_cbranch_scc1 .Lmp0_fb_nomask
	v_cmp_gt_i32_e32 vcc, s8, v224
	s_nop 1
	v_cndmask_b32_e32 v226, 0, v226, vcc
	v_cndmask_b32_e32 v227, 0, v227, vcc
	v_cndmask_b32_e32 v228, 0, v228, vcc
	v_cndmask_b32_e32 v229, 0, v229, vcc

	.amdhsa_kernel _Z10mp2_kernelILb0ELi0EEvPKDF16_PDF16_PKiPKfPKDv8_DF16_S6_S6_ii
		.amdhsa_group_segment_fixed_size 0
		.amdhsa_private_segment_fixed_size 0
		.amdhsa_kernarg_size 320
		.amdhsa_user_sgpr_count 2
		.amdhsa_user_sgpr_dispatch_ptr 0
		.amdhsa_user_sgpr_queue_ptr 0
		.amdhsa_user_sgpr_kernarg_segment_ptr 1
		.amdhsa_user_sgpr_dispatch_id 0
		.amdhsa_user_sgpr_kernarg_preload_length 0
		.amdhsa_user_sgpr_kernarg_preload_offset 0
		.amdhsa_user_sgpr_private_segment_size 0
		.amdhsa_uses_dynamic_stack 0
		.amdhsa_enable_private_segment 0
		.amdhsa_system_sgpr_workgroup_id_x 1
		.amdhsa_system_sgpr_workgroup_id_y 0
		.amdhsa_system_sgpr_workgroup_id_z 0
		.amdhsa_system_sgpr_workgroup_info 0
		.amdhsa_system_vgpr_workitem_id 0
		.amdhsa_next_free_vgpr 252
		.amdhsa_next_free_sgpr 48
		.amdhsa_accum_offset 252
		.amdhsa_reserve_vcc 1
		.amdhsa_float_round_mode_32 0
		.amdhsa_float_round_mode_16_64 0
		.amdhsa_float_denorm_mode_32 3
		.amdhsa_float_denorm_mode_16_64 3
		.amdhsa_dx10_clamp 1
		.amdhsa_ieee_mode 1
		.amdhsa_fp16_overflow 0
		.amdhsa_tg_split 0
		.amdhsa_exception_fp_ieee_invalid_op 0
		.amdhsa_exception_fp_denorm_src 0
		.amdhsa_exception_fp_ieee_div_zero 0
		.amdhsa_exception_fp_ieee_overflow 0
		.amdhsa_exception_fp_ieee_underflow 0
		.amdhsa_exception_fp_ieee_inexact 0
		.amdhsa_exception_int_div_zero 0
	.end_amdhsa_kernel

amdhsa.kernels:
  - .agpr_count:     0
    .args:
      - .actual_access:  write_only
        .address_space:  global
        .offset:         0
        .size:           8
        .value_kind:     global_buffer
      - .actual_access:  read_only
        .address_space:  global
        .offset:         8
        .size:           8
        .value_kind:     global_buffer
      - .actual_access:  read_only
        .address_space:  global
        .offset:         16
        .size:           8
        .value_kind:     global_buffer
      - .actual_access:  read_only
        .address_space:  global
        .offset:         24
        .size:           8
        .value_kind:     global_buffer
      - .actual_access:  read_only
        .address_space:  global
        .offset:         32
        .size:           8
        .value_kind:     global_buffer
      - .actual_access:  read_only
        .address_space:  global
        .offset:         40
        .size:           8
        .value_kind:     global_buffer
      - .actual_access:  read_only
        .address_space:  global
        .offset:         48
        .size:           8
        .value_kind:     global_buffer
      - .actual_access:  read_only
        .address_space:  global
        .offset:         56
        .size:           8
        .value_kind:     global_buffer
      - .actual_access:  read_only
        .address_space:  global
        .offset:         64
        .size:           8
        .value_kind:     global_buffer
      - .actual_access:  read_only
        .address_space:  global
        .offset:         72
        .size:           8
        .value_kind:     global_buffer
    .group_segment_fixed_size: 0
    .kernarg_segment_align: 8
    .kernarg_segment_size: 80
    .language:       OpenCL C
    .language_version:
      - 2
      - 0
    .max_flat_workgroup_size: 64
    .name:           _Z11prep_kernelPDv8_DF16_PKfS2_S2_S2_S2_S2_S2_S2_S2_
    .private_segment_fixed_size: 0
    .sgpr_count:     20
    .sgpr_spill_count: 0
    .symbol:         _Z11prep_kernelPDv8_DF16_PKfS2_S2_S2_S2_S2_S2_S2_S2_.kd
    .uniform_work_group_size: 1
    .uses_dynamic_stack: false
    .vgpr_count:     18
    .vgpr_spill_count: 0
    .wavefront_size: 64
  - .agpr_count:     0
    .args:
      - .actual_access:  read_only
        .address_space:  global
        .offset:         0
        .size:           8
        .value_kind:     global_buffer
      - .actual_access:  read_only
        .address_space:  global
        .offset:         8
        .size:           8
        .value_kind:     global_buffer
      - .actual_access:  write_only
        .address_space:  global
        .offset:         16
        .size:           8
        .value_kind:     global_buffer
    .group_segment_fixed_size: 0
    .kernarg_segment_align: 8
    .kernarg_segment_size: 24
    .language:       OpenCL C
    .language_version:
      - 2
      - 0
    .max_flat_workgroup_size: 256
    .name:           _Z11init_kernelPKfS0_PDF16_
    .private_segment_fixed_size: 0
    .sgpr_count:     16
    .sgpr_spill_count: 0
    .symbol:         _Z11init_kernelPKfS0_PDF16_.kd
    .uniform_work_group_size: 1
    .uses_dynamic_stack: false
    .vgpr_count:     118
    .vgpr_spill_count: 0
    .wavefront_size: 64
  - .agpr_count:     0
    .args:
      - .actual_access:  read_only
        .address_space:  global
        .offset:         0
        .size:           8
        .value_kind:     global_buffer
      - .actual_access:  write_only
        .address_space:  global
        .offset:         8
        .size:           8
        .value_kind:     global_buffer
      - .actual_access:  read_only
        .address_space:  global
        .offset:         16
        .size:           8
        .value_kind:     global_buffer
      - .actual_access:  read_only
        .address_space:  global
        .offset:         24
        .size:           8
        .value_kind:     global_buffer
      - .actual_access:  read_only
        .address_space:  global
        .offset:         32
        .size:           8
        .value_kind:     global_buffer
      - .actual_access:  read_only
        .address_space:  global
        .offset:         40
        .size:           8
        .value_kind:     global_buffer
      - .actual_access:  read_only
        .address_space:  global
        .offset:         48
        .size:           8
        .value_kind:     global_buffer
      - .offset:         56
        .size:           4
        .value_kind:     by_value
      - .offset:         64
        .size:           4
        .value_kind:     hidden_block_count_x
      - .offset:         68
        .size:           4
        .value_kind:     hidden_block_count_y
      - .offset:         72
        .size:           4
        .value_kind:     hidden_block_count_z
      - .offset:         76
        .size:           2
        .value_kind:     hidden_group_size_x
      - .offset:         78
        .size:           2
        .value_kind:     hidden_group_size_y
      - .offset:         80
        .size:           2
        .value_kind:     hidden_group_size_z
      - .offset:         82
        .size:           2
        .value_kind:     hidden_remainder_x
      - .offset:         84
        .size:           2
        .value_kind:     hidden_remainder_y
      - .offset:         86
        .size:           2
        .value_kind:     hidden_remainder_z
      - .offset:         104
        .size:           8
        .value_kind:     hidden_global_offset_x
      - .offset:         112
        .size:           8
        .value_kind:     hidden_global_offset_y
      - .offset:         120
        .size:           8
        .value_kind:     hidden_global_offset_z
      - .offset:         128
        .size:           2
        .value_kind:     hidden_grid_dims
      - .offset:         184
        .size:           4
        .value_kind:     hidden_dynamic_lds_size
    .group_segment_fixed_size: 0
    .kernarg_segment_align: 8
    .kernarg_segment_size: 320
    .language:       OpenCL C
    .language_version:
      - 2
      - 0
    .max_flat_workgroup_size: 512
    .name:           _Z12xproj_kernelPKDF16_PDF16_PKDv8_DF16_PKfS6_S6_S6_i
    .private_segment_fixed_size: 0
    .sgpr_count:     30
    .sgpr_spill_count: 0
    .symbol:         _Z12xproj_kernelPKDF16_PDF16_PKDv8_DF16_PKfS6_S6_S6_i.kd
    .uniform_work_group_size: 1
    .uses_dynamic_stack: false
    .vgpr_count:     16
    .vgpr_spill_count: 0
    .wavefront_size: 64
  - .agpr_count:     0
    .args:
      - .actual_access:  read_only
        .address_space:  global
        .offset:         0
        .size:           8
        .value_kind:     global_buffer
      - .actual_access:  read_only
        .address_space:  global
        .offset:         8
        .size:           8
        .value_kind:     global_buffer
      - .actual_access:  write_only
        .address_space:  global
        .offset:         16
        .size:           8
        .value_kind:     global_buffer
    .group_segment_fixed_size: 5120
    .kernarg_segment_align: 8
    .kernarg_segment_size: 24
    .language:       OpenCL C
    .language_version:
      - 2
      - 0
    .max_flat_workgroup_size: 1024
    .name:           _Z11lstm_kernelPKDF16_PKDv8_DF16_Pf
    .private_segment_fixed_size: 0
    .sgpr_count:     18
    .sgpr_spill_count: 0
    .symbol:         _Z11lstm_kernelPKDF16_PKDv8_DF16_Pf.kd
    .uniform_work_group_size: 1
    .uses_dynamic_stack: false
    .vgpr_count:     52
    .vgpr_spill_count: 0
    .wavefront_size: 64
  - .agpr_count:     0
    .args:
      - .actual_access:  read_only
        .address_space:  global
        .offset:         0
        .size:           8
        .value_kind:     global_buffer
      - .actual_access:  read_only
        .address_space:  global
        .offset:         8
        .size:           8
        .value_kind:     global_buffer
      - .actual_access:  write_only
        .address_space:  global
        .offset:         16
        .size:           8
        .value_kind:     global_buffer
    .group_segment_fixed_size: 36096
    .kernarg_segment_align: 8
    .kernarg_segment_size: 24
    .language:       OpenCL C
    .language_version:
      - 2
      - 0
    .max_flat_workgroup_size: 256
    .name:           _Z12lstm2_kernelPKDF16_PKDv8_DF16_Pf
    .private_segment_fixed_size: 0
    .sgpr_count:     38
    .sgpr_spill_count: 0
    .symbol:         _Z12lstm2_kernelPKDF16_PKDv8_DF16_Pf.kd
    .uniform_work_group_size: 1
    .uses_dynamic_stack: false
    .vgpr_count:     252
    .vgpr_spill_count: 0
    .wavefront_size: 64
  - .agpr_count:     0
    .args:
      - .address_space:  global
        .offset:         0
        .size:           8
        .value_kind:     global_buffer
      - .actual_access:  write_only
        .address_space:  global
        .offset:         8
        .size:           8
        .value_kind:     global_buffer
      - .address_space:  global
        .offset:         16
        .size:           8
        .value_kind:     global_buffer
      - .address_space:  global
        .offset:         24
        .size:           8
        .value_kind:     global_buffer
      - .actual_access:  read_only
        .address_space:  global
        .offset:         32
        .size:           8
        .value_kind:     global_buffer
      - .actual_access:  read_only
        .address_space:  global
        .offset:         40
        .size:           8
        .value_kind:     global_buffer
      - .actual_access:  read_only
        .address_space:  global
        .offset:         48
        .size:           8
        .value_kind:     global_buffer
      - .offset:         56
        .size:           4
        .value_kind:     by_value
      - .offset:         60
        .size:           4
        .value_kind:     by_value
      - .offset:         64
        .size:           4
        .value_kind:     hidden_block_count_x
      - .offset:         68
        .size:           4
        .value_kind:     hidden_block_count_y
      - .offset:         72
        .size:           4
        .value_kind:     hidden_block_count_z
      - .offset:         76
        .size:           2
        .value_kind:     hidden_group_size_x
      - .offset:         78
        .size:           2
        .value_kind:     hidden_group_size_y
      - .offset:         80
        .size:           2
        .value_kind:     hidden_group_size_z
      - .offset:         82
        .size:           2
        .value_kind:     hidden_remainder_x
      - .offset:         84
        .size:           2
        .value_kind:     hidden_remainder_y
      - .offset:         86
        .size:           2
        .value_kind:     hidden_remainder_z
      - .offset:         104
        .size:           8
        .value_kind:     hidden_global_offset_x
      - .offset:         112
        .size:           8
        .value_kind:     hidden_global_offset_y
      - .offset:         120
        .size:           8
        .value_kind:     hidden_global_offset_z
      - .offset:         128
        .size:           2
        .value_kind:     hidden_grid_dims
      - .offset:         184
        .size:           4
        .value_kind:     hidden_dynamic_lds_size
    .group_segment_fixed_size: 0
    .kernarg_segment_align: 8
    .kernarg_segment_size: 320
    .language:       OpenCL C
    .language_version:
      - 2
      - 0
    .max_flat_workgroup_size: 512
    .name:           _Z10mp2_kernelILb0ELi0EEvPKDF16_PDF16_PKiPKfPKDv8_DF16_S6_S6_ii
    .private_segment_fixed_size: 0
    .sgpr_count:     54
    .sgpr_spill_count: 0
    .symbol:         _Z10mp2_kernelILb0ELi0EEvPKDF16_PDF16_PKiPKfPKDv8_DF16_S6_S6_ii.kd
    .uniform_work_group_size: 1
    .uses_dynamic_stack: false
    .vgpr_count:     252
    .vgpr_spill_count: 0
    .wavefront_size: 64
  - .agpr_count:     0
    .args:
      - .actual_access:  read_only
        .address_space:  global
        .offset:         0
        .size:           8
        .value_kind:     global_buffer
      - .actual_access:  write_only
        .address_space:  global
        .offset:         8
        .size:           8
        .value_kind:     global_buffer
      - .address_space:  global
        .offset:         16
        .size:           8
        .value_kind:     global_buffer
      - .address_space:  global
        .offset:         24
        .size:           8
        .value_kind:     global_buffer
      - .actual_access:  read_only
        .address_space:  global
        .offset:         32
        .size:           8
        .value_kind:     global_buffer
      - .actual_access:  read_only
        .address_space:  global
        .offset:         40
        .size:           8
        .value_kind:     global_buffer
      - .actual_access:  read_only
        .address_space:  global
        .offset:         48
        .size:           8
        .value_kind:     global_buffer
      - .offset:         56
        .size:           4
        .value_kind:     by_value
      - .offset:         60
        .size:           4
        .value_kind:     by_value
      - .offset:         64
        .size:           4
        .value_kind:     hidden_block_count_x
      - .offset:         68
        .size:           4
        .value_kind:     hidden_block_count_y
      - .offset:         72
        .size:           4
        .value_kind:     hidden_block_count_z
      - .offset:         76
        .size:           2
        .value_kind:     hidden_group_size_x
      - .offset:         78
        .size:           2
        .value_kind:     hidden_group_size_y
      - .offset:         80
        .size:           2
        .value_kind:     hidden_group_size_z
      - .offset:         82
        .size:           2
        .value_kind:     hidden_remainder_x
      - .offset:         84
        .size:           2
        .value_kind:     hidden_remainder_y
      - .offset:         86
        .size:           2
        .value_kind:     hidden_remainder_z
      - .offset:         104
        .size:           8
        .value_kind:     hidden_global_offset_x
      - .offset:         112
        .size:           8
        .value_kind:     hidden_global_offset_y
      - .offset:         120
        .size:           8
        .value_kind:     hidden_global_offset_z
      - .offset:         128
        .size:           2
        .value_kind:     hidden_grid_dims
      - .offset:         184
        .size:           4
        .value_kind:     hidden_dynamic_lds_size
    .group_segment_fixed_size: 0
    .kernarg_segment_align: 8
    .kernarg_segment_size: 320
    .language:       OpenCL C
    .language_version:
      - 2
      - 0
    .max_flat_workgroup_size: 512
    .name:           _Z10mp2_kernelILb0ELi1EEvPKDF16_PDF16_PKiPKfPKDv8_DF16_S6_S6_ii
    .private_segment_fixed_size: 0
    .sgpr_count:     32
    .sgpr_spill_count: 0
    .symbol:         _Z10mp2_kernelILb0ELi1EEvPKDF16_PDF16_PKiPKfPKDv8_DF16_S6_S6_ii.kd
    .uniform_work_group_size: 1
    .uses_dynamic_stack: false
    .vgpr_count:     234
    .vgpr_spill_count: 0
    .wavefront_size: 64
  - .agpr_count:     0
    .args:
      - .address_space:  global
        .offset:         0
        .size:           8
        .value_kind:     global_buffer
      - .actual_access:  write_only
        .address_space:  global
        .offset:         8
        .size:           8
        .value_kind:     global_buffer
      - .actual_access:  read_only
        .address_space:  global
        .offset:         16
        .size:           8
        .value_kind:     global_buffer
      - .actual_access:  read_only
        .address_space:  global
        .offset:         24
        .size:           8
        .value_kind:     global_buffer
      - .actual_access:  read_only
        .address_space:  global
        .offset:         32
        .size:           8
        .value_kind:     global_buffer
      - .actual_access:  read_only
        .address_space:  global
        .offset:         40
        .size:           8
        .value_kind:     global_buffer
      - .actual_access:  read_only
        .address_space:  global
        .offset:         48
        .size:           8
        .value_kind:     global_buffer
      - .offset:         56
        .size:           4
        .value_kind:     by_value
      - .offset:         60
        .size:           4
        .value_kind:     by_value
      - .offset:         64
        .size:           4
        .value_kind:     hidden_block_count_x
      - .offset:         68
        .size:           4
        .value_kind:     hidden_block_count_y
      - .offset:         72
        .size:           4
        .value_kind:     hidden_block_count_z
      - .offset:         76
        .size:           2
        .value_kind:     hidden_group_size_x
      - .offset:         78
        .size:           2
        .value_kind:     hidden_group_size_y
      - .offset:         80
        .size:           2
        .value_kind:     hidden_group_size_z
      - .offset:         82
        .size:           2
        .value_kind:     hidden_remainder_x
      - .offset:         84
        .size:           2
        .value_kind:     hidden_remainder_y
      - .offset:         86
        .size:           2
        .value_kind:     hidden_remainder_z
      - .offset:         104
        .size:           8
        .value_kind:     hidden_global_offset_x
      - .offset:         112
        .size:           8
        .value_kind:     hidden_global_offset_y
      - .offset:         120
        .size:           8
        .value_kind:     hidden_global_offset_z
      - .offset:         128
        .size:           2
        .value_kind:     hidden_grid_dims
      - .offset:         184
        .size:           4
        .value_kind:     hidden_dynamic_lds_size
    .group_segment_fixed_size: 0
    .kernarg_segment_align: 8
    .kernarg_segment_size: 320
    .language:       OpenCL C
    .language_version:
      - 2
      - 0
    .max_flat_workgroup_size: 512
    .name:           _Z9mp_kernelILi1EEvPKDF16_PDF16_PKiPKfPKDv8_DF16_S6_S6_ii
    .private_segment_fixed_size: 0
    .sgpr_count:     46
    .sgpr_spill_count: 0
    .symbol:         _Z9mp_kernelILi1EEvPKDF16_PDF16_PKiPKfPKDv8_DF16_S6_S6_ii.kd
    .uniform_work_group_size: 1
    .uses_dynamic_stack: false
    .vgpr_count:     70
    .vgpr_spill_count: 0
    .wavefront_size: 64
  - .agpr_count:     0
    .args:
      - .address_space:  global
        .offset:         0
        .size:           8
        .value_kind:     global_buffer
      - .actual_access:  write_only
        .address_space:  global
        .offset:         8
        .size:           8
        .value_kind:     global_buffer
      - .address_space:  global
        .offset:         16
        .size:           8
        .value_kind:     global_buffer
      - .address_space:  global
        .offset:         24
        .size:           8
        .value_kind:     global_buffer
      - .actual_access:  read_only
        .address_space:  global
        .offset:         32
        .size:           8
        .value_kind:     global_buffer
      - .actual_access:  read_only
        .address_space:  global
        .offset:         40
        .size:           8
        .value_kind:     global_buffer
      - .actual_access:  read_only
        .address_space:  global
        .offset:         48
        .size:           8
        .value_kind:     global_buffer
      - .offset:         56
        .size:           4
        .value_kind:     by_value
      - .offset:         60
        .size:           4
        .value_kind:     by_value
      - .offset:         64
        .size:           4
        .value_kind:     hidden_block_count_x
      - .offset:         68
        .size:           4
        .value_kind:     hidden_block_count_y
      - .offset:         72
        .size:           4
        .value_kind:     hidden_block_count_z
      - .offset:         76
        .size:           2
        .value_kind:     hidden_group_size_x
      - .offset:         78
        .size:           2
        .value_kind:     hidden_group_size_y
      - .offset:         80
        .size:           2
        .value_kind:     hidden_group_size_z
      - .offset:         82
        .size:           2
        .value_kind:     hidden_remainder_x
      - .offset:         84
        .size:           2
        .value_kind:     hidden_remainder_y
      - .offset:         86
        .size:           2
        .value_kind:     hidden_remainder_z
      - .offset:         104
        .size:           8
        .value_kind:     hidden_global_offset_x
      - .offset:         112
        .size:           8
        .value_kind:     hidden_global_offset_y
      - .offset:         120
        .size:           8
        .value_kind:     hidden_global_offset_z
      - .offset:         128
        .size:           2
        .value_kind:     hidden_grid_dims
      - .offset:         184
        .size:           4
        .value_kind:     hidden_dynamic_lds_size
    .group_segment_fixed_size: 0
    .kernarg_segment_align: 8
    .kernarg_segment_size: 320
    .language:       OpenCL C
    .language_version:
      - 2
      - 0
    .max_flat_workgroup_size: 512
    .name:           _Z10mp2_kernelILb0ELi2EEvPKDF16_PDF16_PKiPKfPKDv8_DF16_S6_S6_ii
    .private_segment_fixed_size: 0
    .sgpr_count:     34
    .sgpr_spill_count: 0
    .symbol:         _Z10mp2_kernelILb0ELi2EEvPKDF16_PDF16_PKiPKfPKDv8_DF16_S6_S6_ii.kd
    .uniform_work_group_size: 1
    .uses_dynamic_stack: false
    .vgpr_count:     99
    .vgpr_spill_count: 0
    .wavefront_size: 64
